# PEER V second half: row prefetch issued behind the token-start loads so one counted vmcnt(16) covers them; the token-end vmcnt(0) drain of the prefetch is gone
# baseline (speedup 1.0000x reference)
.Lpv_go2:
	s_max_u32 s38, s38, s70
	s_lshl_b32 s48, s59, 4
	s_cmp_ge_i32 s48, s30
	s_cselect_b64 s[52:53], -1, 0
	s_cmp_lt_i32 s48, s39
	s_cselect_b64 s[54:55], -1, 0
	s_waitcnt lgkmcnt(0)
	s_and_b64 vcc, s[52:53], s[54:55]
	s_cselect_b32 s54, 0x45000000, 0
	v_mul_f32_e32 v1, s54, v178
	v_cvt_pk_fp8_f32 v2, v1, v1
	v_mul_f32_e32 v177, s54, v179
	v_cvt_pk_fp8_f32 v178, v177, v177
	v_perm_b32 v2, v2, v2, v249
	v_mov_b32_e32 v3, v0
	s_nop 1
	v_mfma_f32_16x16x32_fp8_fp8 v[160:163], v[2:3], v[4:5], v[160:163]
	v_mov_b32_e32 v1, v2
	v_mul_f32_e32 v177, s54, v180
	v_mfma_f32_16x16x32_fp8_fp8 v[152:155], v[2:3], v[6:7], v[152:155]
	v_perm_b32 v2, v178, v178, v249
	v_cvt_pk_fp8_f32 v178, v177, v177
	v_mfma_f32_16x16x32_fp8_fp8 v[164:167], v[0:1], v[4:5], v[164:167]
	v_mfma_f32_16x16x32_fp8_fp8 v[156:159], v[0:1], v[6:7], v[156:159]
	v_mov_b32_e32 v1, v2
	v_mfma_f32_16x16x32_fp8_fp8 v[160:163], v[2:3], v[8:9], v[160:163]
	v_mfma_f32_16x16x32_fp8_fp8 v[152:155], v[2:3], v[10:11], v[152:155]
	v_perm_b32 v2, v178, v178, v249
	s_nop 0
	s_nop 0
	v_mfma_f32_16x16x32_fp8_fp8 v[182:185], v[2:3], v[12:13], v[160:163]
	s_nop 1
	s_nop 1
	v_mul_f32_e32 v177, s54, v181
	v_cvt_pk_fp8_f32 v178, v177, v177
	v_mfma_f32_16x16x32_fp8_fp8 v[164:167], v[0:1], v[8:9], v[164:167]
	v_mfma_f32_16x16x32_fp8_fp8 v[156:159], v[0:1], v[10:11], v[156:159]
	v_mov_b32_e32 v1, v2
	v_mfma_f32_16x16x32_fp8_fp8 v[160:163], v[2:3], v[14:15], v[152:155]
	v_perm_b32 v2, v178, v178, v249
	ds_read_b128 v[178:181], v176 offset:16
	v_mfma_f32_16x16x32_fp8_fp8 v[164:167], v[0:1], v[12:13], v[164:167]
	s_waitcnt lgkmcnt(0)
	v_mul_f32_e32 v177, s54, v178
	v_cvt_pk_fp8_f32 v178, v177, v177
	v_mfma_f32_16x16x32_fp8_fp8 v[156:159], v[0:1], v[14:15], v[156:159]
	v_mov_b32_e32 v1, v2
	v_mfma_f32_16x16x32_fp8_fp8 v[152:155], v[2:3], v[16:17], v[182:185]
	v_mul_f32_e32 v177, s54, v179
	v_mfma_f32_16x16x32_fp8_fp8 v[160:163], v[2:3], v[18:19], v[160:163]
	v_perm_b32 v2, v178, v178, v249
	v_cvt_pk_fp8_f32 v178, v177, v177
	v_mfma_f32_16x16x32_fp8_fp8 v[164:167], v[0:1], v[16:17], v[164:167]
	v_mul_f32_e32 v177, s54, v180
	v_mfma_f32_16x16x32_fp8_fp8 v[156:159], v[0:1], v[18:19], v[156:159]
	v_mov_b32_e32 v1, v2
	v_mfma_f32_16x16x32_fp8_fp8 v[152:155], v[2:3], v[20:21], v[152:155]
	v_mfma_f32_16x16x32_fp8_fp8 v[160:163], v[2:3], v[22:23], v[160:163]
	v_perm_b32 v2, v178, v178, v249
	v_cvt_pk_fp8_f32 v178, v177, v177
	v_mfma_f32_16x16x32_fp8_fp8 v[164:167], v[0:1], v[20:21], v[164:167]
	v_mfma_f32_16x16x32_fp8_fp8 v[156:159], v[0:1], v[22:23], v[156:159]
	v_mov_b32_e32 v1, v2
	v_mul_f32_e32 v177, s54, v181
	v_mfma_f32_16x16x32_fp8_fp8 v[152:155], v[2:3], v[24:25], v[152:155]
	v_mfma_f32_16x16x32_fp8_fp8 v[160:163], v[2:3], v[26:27], v[160:163]
	v_perm_b32 v2, v178, v178, v249
	v_cvt_pk_fp8_f32 v178, v177, v177
	v_mfma_f32_16x16x32_fp8_fp8 v[164:167], v[0:1], v[24:25], v[164:167]
	v_mfma_f32_16x16x32_fp8_fp8 v[156:159], v[0:1], v[26:27], v[156:159]
	v_mov_b32_e32 v1, v2
	v_mfma_f32_16x16x32_fp8_fp8 v[152:155], v[2:3], v[28:29], v[152:155]
	v_mfma_f32_16x16x32_fp8_fp8 v[160:163], v[2:3], v[30:31], v[160:163]
	v_perm_b32 v2, v178, v178, v249
	ds_read_b128 v[178:181], v176 offset:32
	s_waitcnt lgkmcnt(0)
	v_mul_f32_e32 v177, s54, v178
	v_cvt_pk_fp8_f32 v178, v177, v177
	v_mfma_f32_16x16x32_fp8_fp8 v[164:167], v[0:1], v[28:29], v[164:167]
	v_mfma_f32_16x16x32_fp8_fp8 v[156:159], v[0:1], v[30:31], v[156:159]
	v_mov_b32_e32 v1, v2
	v_mul_f32_e32 v177, s54, v179
	v_mfma_f32_16x16x32_fp8_fp8 v[152:155], v[2:3], v[32:33], v[152:155]
	v_mfma_f32_16x16x32_fp8_fp8 v[160:163], v[2:3], v[34:35], v[160:163]
	v_perm_b32 v2, v178, v178, v249
	v_cvt_pk_fp8_f32 v178, v177, v177
	v_mfma_f32_16x16x32_fp8_fp8 v[164:167], v[0:1], v[32:33], v[164:167]
	v_mfma_f32_16x16x32_fp8_fp8 v[156:159], v[0:1], v[34:35], v[156:159]
	v_mov_b32_e32 v1, v2
	v_mul_f32_e32 v177, s54, v180
	v_mfma_f32_16x16x32_fp8_fp8 v[152:155], v[2:3], v[36:37], v[152:155]
	v_mfma_f32_16x16x32_fp8_fp8 v[160:163], v[2:3], v[38:39], v[160:163]
	v_perm_b32 v2, v178, v178, v249
	v_cvt_pk_fp8_f32 v178, v177, v177
	v_mfma_f32_16x16x32_fp8_fp8 v[164:167], v[0:1], v[36:37], v[164:167]
	v_mfma_f32_16x16x32_fp8_fp8 v[156:159], v[0:1], v[38:39], v[156:159]
	v_mov_b32_e32 v1, v2
	v_mul_f32_e32 v177, s54, v181
	v_mfma_f32_16x16x32_fp8_fp8 v[152:155], v[2:3], v[40:41], v[152:155]
	v_mfma_f32_16x16x32_fp8_fp8 v[160:163], v[2:3], v[42:43], v[160:163]
	v_perm_b32 v2, v178, v178, v249
	v_cvt_pk_fp8_f32 v178, v177, v177
	v_mfma_f32_16x16x32_fp8_fp8 v[164:167], v[0:1], v[40:41], v[164:167]
	v_mfma_f32_16x16x32_fp8_fp8 v[156:159], v[0:1], v[42:43], v[156:159]
	v_mov_b32_e32 v1, v2
	v_mfma_f32_16x16x32_fp8_fp8 v[152:155], v[2:3], v[44:45], v[152:155]
	v_mfma_f32_16x16x32_fp8_fp8 v[160:163], v[2:3], v[46:47], v[160:163]
	v_perm_b32 v2, v178, v178, v249
	ds_read_b128 v[176:179], v176 offset:48
	v_mfma_f32_16x16x32_fp8_fp8 v[164:167], v[0:1], v[44:45], v[164:167]
	s_waitcnt lgkmcnt(0)
	v_mul_f32_e32 v176, s54, v176
	v_cvt_pk_fp8_f32 v180, v176, v176
	v_mfma_f32_16x16x32_fp8_fp8 v[156:159], v[0:1], v[46:47], v[156:159]
	v_mov_b32_e32 v1, v2
	v_mul_f32_e32 v176, s54, v177
	v_cvt_pk_fp8_f32 v177, v176, v176
	v_mfma_f32_16x16x32_fp8_fp8 v[152:155], v[2:3], v[48:49], v[152:155]
	v_mfma_f32_16x16x32_fp8_fp8 v[160:163], v[2:3], v[50:51], v[160:163]
	v_perm_b32 v2, v180, v180, v249
	v_mfma_f32_16x16x32_fp8_fp8 v[164:167], v[0:1], v[48:49], v[164:167]
	v_mul_f32_e32 v176, s54, v178
	v_mfma_f32_16x16x32_fp8_fp8 v[156:159], v[0:1], v[50:51], v[156:159]
	v_mov_b32_e32 v1, v2
	v_mfma_f32_16x16x32_fp8_fp8 v[152:155], v[2:3], v[52:53], v[152:155]
	s_add_i32 s38, s38, -1
	v_mfma_f32_16x16x32_fp8_fp8 v[160:163], v[2:3], v[54:55], v[160:163]
	v_perm_b32 v2, v177, v177, v249
	v_cvt_pk_fp8_f32 v177, v176, v176
	v_mfma_f32_16x16x32_fp8_fp8 v[164:167], v[0:1], v[52:53], v[164:167]
	s_cmp_lg_u32 s59, s38
	v_mfma_f32_16x16x32_fp8_fp8 v[156:159], v[0:1], v[54:55], v[156:159]
	v_mov_b32_e32 v1, v2
	v_mul_f32_e32 v180, s54, v179
	v_cvt_pk_fp8_f32 v181, v180, v180
	v_mfma_f32_16x16x32_fp8_fp8 v[152:155], v[2:3], v[56:57], v[152:155]
	v_mfma_f32_16x16x32_fp8_fp8 v[160:163], v[2:3], v[58:59], v[160:163]
	v_perm_b32 v2, v177, v177, v249
	v_mfma_f32_16x16x32_fp8_fp8 v[164:167], v[0:1], v[56:57], v[164:167]
	v_mfma_f32_16x16x32_fp8_fp8 v[156:159], v[0:1], v[58:59], v[156:159]
	v_mov_b32_e32 v1, v2
	v_mfma_f32_16x16x32_fp8_fp8 v[152:155], v[2:3], v[60:61], v[152:155]
	v_mfma_f32_16x16x32_fp8_fp8 v[176:179], v[2:3], v[62:63], v[160:163]
	v_perm_b32 v2, v181, v181, v249
	v_mfma_f32_16x16x32_fp8_fp8 v[164:167], v[0:1], v[60:61], v[164:167]
	v_mfma_f32_16x16x32_fp8_fp8 v[156:159], v[0:1], v[62:63], v[156:159]
	v_mov_b32_e32 v1, v2
	v_mfma_f32_16x16x32_fp8_fp8 v[160:163], v[2:3], v[64:65], v[152:155]
	s_nop 0
	v_mfma_f32_16x16x32_fp8_fp8 v[164:167], v[0:1], v[64:65], v[164:167]
	v_mfma_f32_16x16x32_fp8_fp8 v[152:155], v[2:3], v[66:67], v[176:179]
	v_mfma_f32_16x16x32_fp8_fp8 v[156:159], v[0:1], v[66:67], v[156:159]
	s_cbranch_scc1 .LBB0_1850
; __device__ __forceinline__ void peer_token_end(Frame& F, const Args& a, int layer, bool last, bool final_half, size_t tok, int lane, const f32x2 (&out)[8], const f32x4 (&hpre)[4], const v4u (&gpre)[2], const v4u& p8pre) {
;     float* hp = F.h + tok * 1024 + 16 * lane;
;     f32x4 hv[4], ge[4]; float s = 0.f;
;     f32x4 pe[4];
; #pragma unroll
;     for (int i = 0; i < 4; ++i) { const f32x2 lo = __builtin_amdgcn_cvt_pk_f32_fp8((int)p8pre[i], false), hi = __builtin_amdgcn_cvt_pk_f32_fp8((int)p8pre[i], true);
;         pe[i] = (f32x4){lo.x, lo.y, hi.x, hi.y} * (1.f / 256.f) + (f32x4){out[2 * i].x, out[2 * i].y, out[2 * i + 1].x, out[2 * i + 1].y}; }
;     if (!final_half) {
;         v4u w;
; #pragma unroll
;         for (int i = 0; i < 4; ++i) { const f32x4 s8 = pe[i] * 256.f; int t = 0; t = __builtin_amdgcn_cvt_pk_fp8_f32(s8.x, s8.y, t, false); t = __builtin_amdgcn_cvt_pk_fp8_f32(s8.z, s8.w, t, true); w[i] = (unsigned)t; }
;         *(v4u*)((unsigned char*)(F.ws + WS_P8) + tok * 1024 + 16 * lane) = w;
;         return; }
	s_nop 0
	v_cvt_pk_f32_fp8_e32 v[2:3], v140
	v_cvt_pk_f32_fp8_e32 v[178:179], v141
	v_cvt_pk_f32_fp8_sdwa v[180:181], v141 src0_sel:WORD_1
	v_cvt_pk_f32_fp8_sdwa v[188:189], v142 src0_sel:WORD_1
	v_pk_mul_f32 v[2:3], v[2:3], s[12:13] op_sel_hi:[1,0]
	v_cvt_pk_f32_fp8_e32 v[186:187], v142
	v_pk_fma_f32 v[182:183], v[160:161], s[14:15], v[2:3] op_sel_hi:[1,0,1]
	v_pk_mul_f32 v[2:3], v[178:179], s[12:13] op_sel_hi:[1,0]
	v_pk_mul_f32 v[178:179], v[180:181], s[12:13] op_sel_hi:[1,0]
	v_cvt_pk_f32_fp8_sdwa v[176:177], v140 src0_sel:WORD_1
	v_pk_fma_f32 v[180:181], v[166:167], s[14:15], v[178:179] op_sel_hi:[1,0,1]
	v_pk_mul_f32 v[178:179], v[188:189], s[12:13] op_sel_hi:[1,0]
	v_cvt_pk_f32_fp8_e32 v[188:189], v143
	v_cvt_pk_f32_fp8_sdwa v[192:193], v143 src0_sel:WORD_1
	s_ashr_i32 s30, s57, 31
	s_add_u32 s52, s0, s57
	v_pk_fma_f32 v[184:185], v[164:165], s[14:15], v[2:3] op_sel_hi:[1,0,1]
	v_pk_mul_f32 v[2:3], v[186:187], s[12:13] op_sel_hi:[1,0]
	s_addc_u32 s53, s1, s30
	v_pk_mul_f32 v[176:177], v[176:177], s[12:13] op_sel_hi:[1,0]
	v_pk_fma_f32 v[186:187], v[154:155], s[14:15], v[178:179] op_sel_hi:[1,0,1]
	v_pk_fma_f32 v[190:191], v[152:153], s[14:15], v[2:3] op_sel_hi:[1,0,1]
	v_pk_mul_f32 v[2:3], v[188:189], s[12:13] op_sel_hi:[1,0]
	v_pk_mul_f32 v[178:179], v[192:193], s[12:13] op_sel_hi:[1,0]
	s_lshl_b64 s[38:39], s[52:53], 10
	v_pk_fma_f32 v[176:177], v[162:163], s[14:15], v[176:177] op_sel_hi:[1,0,1]
	v_pk_fma_f32 v[188:189], v[158:159], s[14:15], v[178:179] op_sel_hi:[1,0,1]
	v_pk_fma_f32 v[192:193], v[156:157], s[14:15], v[2:3] op_sel_hi:[1,0,1]
	s_andn2_b64 vcc, exec, s[46:47]
	s_mov_b64 s[54:55], -1
	s_cbranch_vccnz .LBB0_1845
	v_pk_mul_f32 v[2:3], v[182:183], s[8:9] op_sel_hi:[1,0]
	v_mov_b32_e32 v194, v0
	v_cvt_pk_fp8_f32 v194, v2, v3
	v_pk_mul_f32 v[2:3], v[184:185], s[8:9] op_sel_hi:[1,0]
	v_mov_b32_e32 v195, v0
	v_cvt_pk_fp8_f32 v195, v2, v3
	v_pk_mul_f32 v[2:3], v[176:177], s[8:9] op_sel_hi:[1,0]
	v_mov_b32_e32 v196, v0
	v_cvt_pk_fp8_f32 v194, v2, v3 op_sel:[0,0,1]
	v_pk_mul_f32 v[2:3], v[180:181], s[8:9] op_sel_hi:[1,0]
	v_mov_b32_e32 v197, v0
	v_cvt_pk_fp8_f32 v195, v2, v3 op_sel:[0,0,1]
	v_pk_mul_f32 v[2:3], v[190:191], s[8:9] op_sel_hi:[1,0]
	s_mov_b64 s[54:55], 0
	v_cvt_pk_fp8_f32 v196, v2, v3
	v_pk_mul_f32 v[2:3], v[192:193], s[8:9] op_sel_hi:[1,0]
	s_nop 0
	v_cvt_pk_fp8_f32 v197, v2, v3
	v_pk_mul_f32 v[2:3], v[186:187], s[8:9] op_sel_hi:[1,0]
	s_nop 0
	v_cvt_pk_fp8_f32 v196, v2, v3 op_sel:[0,0,1]
	v_pk_mul_f32 v[2:3], v[188:189], s[8:9] op_sel_hi:[1,0]
	s_nop 0
	v_cvt_pk_fp8_f32 v197, v2, v3 op_sel:[0,0,1]
	v_lshl_add_u64 v[2:3], v[234:235], 0, s[38:39]
	global_store_dwordx4 v[2:3], v[194:197], off
